# baseline (speedup 1.0000x reference)
.LBB0_29:
	s_or_b64 exec, exec, s[4:5]
	s_mov_b32 s6, 0x9037ab78
	s_mov_b32 s7, 0x3e21eeb6
	s_mov_b32 s4, 0x46cc5e42
	v_mul_f64 v[12:13], v[8:9], v[8:9]
	s_mov_b32 s5, 0xbda907db
	v_mov_b64_e32 v[22:23], s[6:7]
	s_mov_b32 s6, 0xa17f65f6
	v_mul_f64 v[14:15], v[12:13], 0.5
	v_fma_f64 v[24:25], s[4:5], v[12:13], v[22:23]
	s_mov_b32 s7, 0xbe927e4f
	s_mov_b32 s16, 0x19f4ec90
	v_add_f64 v[16:17], -v[14:15], 1.0
	v_fma_f64 v[24:25], v[12:13], v[24:25], s[6:7]
	s_mov_b32 s17, 0x3efa01a0
	s_mov_b32 s18, 0x16c16967
	v_add_f64 v[20:21], -v[16:17], 1.0
	v_fma_f64 v[24:25], v[12:13], v[24:25], s[16:17]
	s_mov_b32 s19, 0xbf56c16c
	s_mov_b32 s20, 0x55555555
	v_add_f64 v[14:15], v[20:21], -v[14:15]
	v_fma_f64 v[24:25], v[12:13], v[24:25], s[18:19]
	s_mov_b32 s21, 0x3fa55555
	v_mul_f64 v[20:21], v[12:13], v[12:13]
	v_fma_f64 v[24:25], v[12:13], v[24:25], s[20:21]
	v_fma_f64 v[14:15], v[8:9], -v[10:11], v[14:15]
	s_mov_b32 s22, 0xb42fdfa7
	v_fmac_f64_e32 v[14:15], v[20:21], v[24:25]
	s_mov_b32 s23, 0xbe5ae600
	s_mov_b32 s24, 0xf9a43bb8
	v_add_f64 v[14:15], v[16:17], v[14:15]
	s_mov_b32 s25, 0x3de5e0b2
	v_mov_b64_e32 v[16:17], s[22:23]
	s_mov_b32 s22, 0x796cde01
	v_fma_f64 v[20:21], s[24:25], v[12:13], v[16:17]
	s_mov_b32 s23, 0x3ec71de3
	s_mov_b32 s26, 0x19e83e5c
	v_fma_f64 v[20:21], v[12:13], v[20:21], s[22:23]
	s_mov_b32 s27, 0xbf2a01a0
	s_mov_b32 s28, 0x11110bb3
	v_fma_f64 v[20:21], v[12:13], v[20:21], s[26:27]
	s_mov_b32 s29, 0x3f811111
	v_fma_f64 v[20:21], v[12:13], v[20:21], s[28:29]
	v_mul_f64 v[24:25], v[8:9], -v[12:13]
	v_mul_f64 v[26:27], v[10:11], 0.5
	v_fmac_f64_e32 v[26:27], v[24:25], v[20:21]
	v_fma_f64 v[10:11], v[12:13], v[26:27], -v[10:11]
	s_mov_b32 s31, 0xbfc55555
	s_mov_b32 s30, s20
	v_fmac_f64_e32 v[10:11], s[30:31], v[24:25]
	v_add_f64 v[8:9], v[8:9], -v[10:11]
	v_and_b32_e32 v10, 1, v3
	v_cmp_eq_u32_e32 vcc, 0, v10
	v_mul_f64 v[10:11], v[6:7], v[6:7]
	v_xor_b32_e32 v9, 0x80000000, v9
	v_mul_f64 v[12:13], v[10:11], 0.5
	v_fmac_f64_e32 v[22:23], s[4:5], v[10:11]
	v_cndmask_b32_e32 v8, v8, v14, vcc
	v_cndmask_b32_e32 v9, v9, v15, vcc
	v_add_f64 v[14:15], -v[12:13], 1.0
	v_fma_f64 v[22:23], v[10:11], v[22:23], s[6:7]
	v_add_f64 v[20:21], -v[14:15], 1.0
	v_fma_f64 v[22:23], v[10:11], v[22:23], s[16:17]
	v_add_f64 v[12:13], v[20:21], -v[12:13]
	v_fma_f64 v[22:23], v[10:11], v[22:23], s[18:19]
	v_mul_f64 v[20:21], v[10:11], v[10:11]
	v_fma_f64 v[22:23], v[10:11], v[22:23], s[20:21]
	v_fma_f64 v[12:13], v[6:7], -v[18:19], v[12:13]
	v_fmac_f64_e32 v[12:13], v[20:21], v[22:23]
	v_fmac_f64_e32 v[16:17], s[24:25], v[10:11]
	v_add_f64 v[12:13], v[14:15], v[12:13]
	v_fma_f64 v[14:15], v[10:11], v[16:17], s[22:23]
	v_fma_f64 v[14:15], v[10:11], v[14:15], s[26:27]
	v_fma_f64 v[14:15], v[10:11], v[14:15], s[28:29]
	v_mul_f64 v[16:17], v[6:7], -v[10:11]
	v_mul_f64 v[20:21], v[18:19], 0.5
	s_brev_b32 s3, 1
	v_lshlrev_b32_e32 v3, 30, v3
	s_movk_i32 s33, 0x1f8
	v_fmac_f64_e32 v[20:21], v[16:17], v[14:15]
	v_bitop3_b32 v3, v9, v3, s3 bitop3:0x78
	v_cmp_class_f64_e64 vcc, v[4:5], s33
	v_mov_b32_e32 v24, 0x7ff80000
	v_fma_f64 v[10:11], v[10:11], v[20:21], -v[18:19]
	v_cndmask_b32_e32 v9, v24, v3, vcc
	v_fmac_f64_e32 v[10:11], s[30:31], v[16:17]
	v_and_b32_e32 v3, 1, v1
	v_add_f64 v[6:7], v[6:7], -v[10:11]
	v_cmp_eq_u32_e64 s[4:5], 0, v3
	v_lshlrev_b32_e32 v1, 30, v1
	v_xor_b32_e32 v1, v1, v5
	v_cndmask_b32_e64 v3, v12, v6, s[4:5]
	v_cndmask_b32_e64 v6, v13, v7, s[4:5]
	v_cndmask_b32_e32 v8, 0, v8, vcc
	v_bitop3_b32 v1, v6, v1, s3 bitop3:0x78
	v_cvt_f32_f64_e32 v4, v[8:9]
	v_mov_b32_e32 v8, s14
	v_mov_b32_e32 v9, s15
	v_cndmask_b32_e32 v6, 0, v3, vcc
	v_cndmask_b32_e32 v7, v24, v1, vcc
	v_ashrrev_i32_e32 v3, 31, v2
	v_cvt_f32_f64_e32 v5, v[6:7]
	v_lshl_add_u64 v[2:3], v[2:3], 3, v[8:9]
	global_store_dwordx2 v[2:3], v[4:5], off sc0 sc1
